# v12 + z GEMM type-0 epilogue rewritten by hand: cvt in place, bpermute lane transpose, quad-contiguous stores, accumulators re-zeroed inside
# speedup vs baseline: 1.0123x; 1.0106x over previous
_Z6mk_fwd4Args:
	s_mov_b32 s101, 0
	s_load_dword s48, s[0:1], 0xb0
	s_add_u32 s4, s0, 0xb0
	s_addc_u32 s5, s1, 0
	v_readfirstlane_b32 s74, v0
	v_writelane_b32 v255, s4, 0
	s_waitcnt lgkmcnt(0)
	s_and_b32 s3, s48, 7
	s_cmp_lg_u32 s3, 0
	v_writelane_b32 v255, s5, 1
	s_mov_b32 s92, s2
	s_cbranch_scc0 .LBB0_18
	v_cmp_gt_u32_e32 vcc, 32, v0
	s_and_saveexec_b64 s[4:5], vcc

.LBB0_498:
	s_ashr_i32 s25, s24, 31
	s_lshl_b64 s[26:27], s[24:25], 19
	s_add_u32 s26, s60, s26
	s_addc_u32 s27, s61, s27
	s_and_b64 s[28:29], s[6:7], exec
	s_cselect_b32 s9, s27, s35
	s_cselect_b32 s25, s26, s34
	s_ashr_i32 s23, s22, 31
	s_lshl_b64 s[28:29], s[22:23], 19
	s_add_u32 s28, s74, s28
	s_addc_u32 s29, s75, s29
	s_and_b64 s[36:37], s[6:7], exec
	s_cselect_b32 s23, s29, s31
	s_cselect_b32 s33, s28, s30
	s_add_u32 s34, s34, 0x40080
	s_addc_u32 s35, s35, 0
	s_add_u32 s38, s30, 0x100
	v_mov_b32_e32 v2, 0
	s_addc_u32 s39, s31, 0
	s_mov_b32 s88, -2
	s_cmp_eq_u32 s101, 1
	s_mov_b32 s101, 0
	s_cbranch_scc1 .LBB0_499
	v_mov_b32_e32 v3, v2
	v_mov_b32_e32 v4, v2
	v_mov_b32_e32 v5, v2
	v_mov_b32_e32 v6, v2
	v_mov_b32_e32 v7, v2
	v_mov_b32_e32 v8, v2
	v_mov_b32_e32 v9, v2
	v_mov_b32_e32 v18, v2
	v_mov_b32_e32 v19, v2
	v_mov_b32_e32 v20, v2
	v_mov_b32_e32 v21, v2
	v_mov_b32_e32 v22, v2
	v_mov_b32_e32 v23, v2
	v_mov_b32_e32 v24, v2
	v_mov_b32_e32 v25, v2
	v_mov_b32_e32 v34, v2
	v_mov_b32_e32 v35, v2
	v_mov_b32_e32 v36, v2
	v_mov_b32_e32 v37, v2
	v_mov_b32_e32 v38, v2
	v_mov_b32_e32 v39, v2
	v_mov_b32_e32 v40, v2
	v_mov_b32_e32 v41, v2
	v_mov_b32_e32 v50, v2
	v_mov_b32_e32 v51, v2
	v_mov_b32_e32 v52, v2
	v_mov_b32_e32 v53, v2
	v_mov_b32_e32 v54, v2
	v_mov_b32_e32 v55, v2
	v_mov_b32_e32 v56, v2
	v_mov_b32_e32 v57, v2
	v_mov_b32_e32 v10, v2
	v_mov_b32_e32 v11, v2
	v_mov_b32_e32 v12, v2
	v_mov_b32_e32 v13, v2
	v_mov_b32_e32 v14, v2
	v_mov_b32_e32 v15, v2
	v_mov_b32_e32 v16, v2
	v_mov_b32_e32 v17, v2
	v_mov_b32_e32 v26, v2
	v_mov_b32_e32 v27, v2
	v_mov_b32_e32 v28, v2
	v_mov_b32_e32 v29, v2
	v_mov_b32_e32 v30, v2
	v_mov_b32_e32 v31, v2
	v_mov_b32_e32 v32, v2
	v_mov_b32_e32 v33, v2
	v_mov_b32_e32 v42, v2
	v_mov_b32_e32 v43, v2
	v_mov_b32_e32 v44, v2
	v_mov_b32_e32 v45, v2
	v_mov_b32_e32 v46, v2
	v_mov_b32_e32 v47, v2
	v_mov_b32_e32 v48, v2
	v_mov_b32_e32 v49, v2
	v_mov_b32_e32 v58, v2
	v_mov_b32_e32 v59, v2
	v_mov_b32_e32 v60, v2
	v_mov_b32_e32 v61, v2
	v_mov_b32_e32 v62, v2
	v_mov_b32_e32 v63, v2
	v_mov_b32_e32 v64, v2
	v_mov_b32_e32 v65, v2
	v_mov_b32_e32 v66, v2
	v_mov_b32_e32 v67, v2
	v_mov_b32_e32 v68, v2
	v_mov_b32_e32 v69, v2
	v_mov_b32_e32 v70, v2
	v_mov_b32_e32 v71, v2
	v_mov_b32_e32 v72, v2
	v_mov_b32_e32 v73, v2
	v_mov_b32_e32 v82, v2
	v_mov_b32_e32 v83, v2
	v_mov_b32_e32 v84, v2
	v_mov_b32_e32 v85, v2
	v_mov_b32_e32 v86, v2
	v_mov_b32_e32 v87, v2
	v_mov_b32_e32 v88, v2
	v_mov_b32_e32 v89, v2
	v_mov_b32_e32 v98, v2
	v_mov_b32_e32 v99, v2
	v_mov_b32_e32 v100, v2
	v_mov_b32_e32 v101, v2
	v_mov_b32_e32 v102, v2
	v_mov_b32_e32 v103, v2
	v_mov_b32_e32 v104, v2
	v_mov_b32_e32 v105, v2
	v_mov_b32_e32 v114, v2
	v_mov_b32_e32 v115, v2
	v_mov_b32_e32 v116, v2
	v_mov_b32_e32 v117, v2
	v_mov_b32_e32 v118, v2
	v_mov_b32_e32 v119, v2
	v_mov_b32_e32 v120, v2
	v_mov_b32_e32 v121, v2
	v_mov_b32_e32 v74, v2
	v_mov_b32_e32 v75, v2
	v_mov_b32_e32 v76, v2
	v_mov_b32_e32 v77, v2
	v_mov_b32_e32 v78, v2
	v_mov_b32_e32 v79, v2
	v_mov_b32_e32 v80, v2
	v_mov_b32_e32 v81, v2
	v_mov_b32_e32 v90, v2
	v_mov_b32_e32 v91, v2
	v_mov_b32_e32 v92, v2
	v_mov_b32_e32 v93, v2
	v_mov_b32_e32 v94, v2
	v_mov_b32_e32 v95, v2
	v_mov_b32_e32 v96, v2
	v_mov_b32_e32 v97, v2
	v_mov_b32_e32 v106, v2
	v_mov_b32_e32 v107, v2
	v_mov_b32_e32 v108, v2
	v_mov_b32_e32 v109, v2
	v_mov_b32_e32 v110, v2
	v_mov_b32_e32 v111, v2
	v_mov_b32_e32 v112, v2
	v_mov_b32_e32 v113, v2
	v_mov_b32_e32 v122, v2
	v_mov_b32_e32 v123, v2
	v_mov_b32_e32 v124, v2
	v_mov_b32_e32 v125, v2
	v_mov_b32_e32 v126, v2
	v_mov_b32_e32 v127, v2
	v_mov_b32_e32 v128, v2
	v_mov_b32_e32 v129, v2

.LBB0_537:
	s_and_b64 vcc, exec, s[34:35]
	s_cbranch_vccz .LBB0_536
	v_lshrrev_b32_e32 v131, 2, v248
	v_and_b32_e32 v136, 3, v248
	v_lshlrev_b32_e32 v130, 6, v136
	v_lshl_add_u32 v130, v131, 2, v130
	v_and_b32_e32 v137, -16, v165
	v_or_b32_e32 v137, v137, v131
	v_add_u32_e32 v137, s9, v137
	s_cmp_lt_i32 s8, 6
	s_cbranch_scc0 .Lz_t0_vtile
	v_mul_u32_u24_e32 v132, 0xc00, v137
	v_lshl_or_b32 v131, v136, 3, s54
	v_lshl_or_b32 v131, s8, 8, v131
	v_lshl_add_u32 v132, v131, 1, v132
	v_mov_b32_e32 v133, 0
	v_lshl_add_u64 v[132:133], s[66:67], 0, v[132:133]
	s_mov_b32 s98, 0x100
	s_mov_b32 s99, 0
	v_lshl_add_u64 v[134:135], v[132:133], 0, s[98:99]
	s_mov_b32 s98, 0xc000
	s_mov_b32 s100, 0x3c000
	s_branch .Lz_t0_go
.Lz_t0_vtile:
	v_lshlrev_b32_e32 v132, 8, v137
	v_lshl_add_u32 v132, v136, 4, v132
	s_lshl_b32 s100, s54, 1
	v_add_u32_e32 v132, s100, v132
	v_mov_b32_e32 v133, 0
	s_lshl_b64 s[98:99], s[30:31], 1
	s_add_u32 s98, s66, s98
	s_addc_u32 s99, s67, s99
	v_lshl_add_u64 v[132:133], s[98:99], 0, v[132:133]
	s_mov_b32 s98, 0x400000
	s_mov_b32 s99, 0
	v_lshl_add_u64 v[134:135], v[132:133], 0, s[98:99]
	s_mov_b32 s98, 0x1000
	s_mov_b32 s100, 0x5000
.Lz_t0_go:
	s_mov_b32 s101, 0
	v_cvt_pk_bf16_f32 v126, v126, v127
	v_cvt_pk_bf16_f32 v127, v128, v129
	v_cvt_pk_bf16_f32 v128, v122, v123
	v_cvt_pk_bf16_f32 v129, v124, v125
	ds_bpermute_b32 v126, v130, v126
	ds_bpermute_b32 v127, v130, v127
	ds_bpermute_b32 v128, v130, v128
	ds_bpermute_b32 v129, v130, v129
	v_mov_b32_e32 v122, 0
	v_mov_b32_e32 v123, 0
	v_mov_b32_e32 v124, 0
	v_mov_b32_e32 v125, 0
	v_cvt_pk_bf16_f32 v118, v118, v119
	v_cvt_pk_bf16_f32 v119, v120, v121
	v_cvt_pk_bf16_f32 v120, v114, v115
	v_cvt_pk_bf16_f32 v121, v116, v117
	ds_bpermute_b32 v118, v130, v118
	ds_bpermute_b32 v119, v130, v119
	ds_bpermute_b32 v120, v130, v120
	ds_bpermute_b32 v121, v130, v121
	v_mov_b32_e32 v114, 0
	v_mov_b32_e32 v115, 0
	v_mov_b32_e32 v116, 0
	v_mov_b32_e32 v117, 0
	s_waitcnt lgkmcnt(4)
	global_store_dwordx4 v[132:133], v[126:129], off
	v_lshl_add_u64 v[132:133], v[132:133], 0, s[98:99]
	v_cvt_pk_bf16_f32 v110, v110, v111
	v_cvt_pk_bf16_f32 v111, v112, v113
	v_cvt_pk_bf16_f32 v112, v106, v107
	v_cvt_pk_bf16_f32 v113, v108, v109
	ds_bpermute_b32 v110, v130, v110
	ds_bpermute_b32 v111, v130, v111
	ds_bpermute_b32 v112, v130, v112
	ds_bpermute_b32 v113, v130, v113
	v_mov_b32_e32 v106, 0
	v_mov_b32_e32 v107, 0
	v_mov_b32_e32 v108, 0
	v_mov_b32_e32 v109, 0
	v_mov_b32_e32 v126, 0
	v_mov_b32_e32 v127, 0
	v_mov_b32_e32 v128, 0
	v_mov_b32_e32 v129, 0
	s_waitcnt lgkmcnt(4)
	global_store_dwordx4 v[134:135], v[118:121], off
	v_lshl_add_u64 v[134:135], v[134:135], 0, s[98:99]
	v_cvt_pk_bf16_f32 v102, v102, v103
	v_cvt_pk_bf16_f32 v103, v104, v105
	v_cvt_pk_bf16_f32 v104, v98, v99
	v_cvt_pk_bf16_f32 v105, v100, v101
	ds_bpermute_b32 v102, v130, v102
	ds_bpermute_b32 v103, v130, v103
	ds_bpermute_b32 v104, v130, v104
	ds_bpermute_b32 v105, v130, v105
	v_mov_b32_e32 v98, 0
	v_mov_b32_e32 v99, 0
	v_mov_b32_e32 v100, 0
	v_mov_b32_e32 v101, 0
	v_mov_b32_e32 v118, 0
	v_mov_b32_e32 v119, 0
	v_mov_b32_e32 v120, 0
	v_mov_b32_e32 v121, 0
	s_waitcnt lgkmcnt(4)
	global_store_dwordx4 v[132:133], v[110:113], off
	v_lshl_add_u64 v[132:133], v[132:133], 0, s[98:99]
	v_cvt_pk_bf16_f32 v94, v94, v95
	v_cvt_pk_bf16_f32 v95, v96, v97
	v_cvt_pk_bf16_f32 v96, v90, v91
	v_cvt_pk_bf16_f32 v97, v92, v93
	ds_bpermute_b32 v94, v130, v94
	ds_bpermute_b32 v95, v130, v95
	ds_bpermute_b32 v96, v130, v96
	ds_bpermute_b32 v97, v130, v97
	v_mov_b32_e32 v90, 0
	v_mov_b32_e32 v91, 0
	v_mov_b32_e32 v92, 0
	v_mov_b32_e32 v93, 0
	v_mov_b32_e32 v110, 0
	v_mov_b32_e32 v111, 0
	v_mov_b32_e32 v112, 0
	v_mov_b32_e32 v113, 0
	s_waitcnt lgkmcnt(4)
	global_store_dwordx4 v[134:135], v[102:105], off
	v_lshl_add_u64 v[134:135], v[134:135], 0, s[98:99]
	v_cvt_pk_bf16_f32 v86, v86, v87
	v_cvt_pk_bf16_f32 v87, v88, v89
	v_cvt_pk_bf16_f32 v88, v82, v83
	v_cvt_pk_bf16_f32 v89, v84, v85
	ds_bpermute_b32 v86, v130, v86
	ds_bpermute_b32 v87, v130, v87
	ds_bpermute_b32 v88, v130, v88
	ds_bpermute_b32 v89, v130, v89
	v_mov_b32_e32 v82, 0
	v_mov_b32_e32 v83, 0
	v_mov_b32_e32 v84, 0
	v_mov_b32_e32 v85, 0
	v_mov_b32_e32 v102, 0
	v_mov_b32_e32 v103, 0
	v_mov_b32_e32 v104, 0
	v_mov_b32_e32 v105, 0
	s_waitcnt lgkmcnt(4)
	global_store_dwordx4 v[132:133], v[94:97], off
	v_lshl_add_u64 v[132:133], v[132:133], 0, s[98:99]
	v_cvt_pk_bf16_f32 v78, v78, v79
	v_cvt_pk_bf16_f32 v79, v80, v81
	v_cvt_pk_bf16_f32 v80, v74, v75
	v_cvt_pk_bf16_f32 v81, v76, v77
	ds_bpermute_b32 v78, v130, v78
	ds_bpermute_b32 v79, v130, v79
	ds_bpermute_b32 v80, v130, v80
	ds_bpermute_b32 v81, v130, v81
	v_mov_b32_e32 v74, 0
	v_mov_b32_e32 v75, 0
	v_mov_b32_e32 v76, 0
	v_mov_b32_e32 v77, 0
	v_mov_b32_e32 v94, 0
	v_mov_b32_e32 v95, 0
	v_mov_b32_e32 v96, 0
	v_mov_b32_e32 v97, 0
	s_waitcnt lgkmcnt(4)
	global_store_dwordx4 v[134:135], v[86:89], off
	v_lshl_add_u64 v[134:135], v[134:135], 0, s[98:99]
	v_cvt_pk_bf16_f32 v70, v70, v71
	v_cvt_pk_bf16_f32 v71, v72, v73
	v_cvt_pk_bf16_f32 v72, v66, v67
	v_cvt_pk_bf16_f32 v73, v68, v69
	ds_bpermute_b32 v70, v130, v70
	ds_bpermute_b32 v71, v130, v71
	ds_bpermute_b32 v72, v130, v72
	ds_bpermute_b32 v73, v130, v73
	v_mov_b32_e32 v66, 0
	v_mov_b32_e32 v67, 0
	v_mov_b32_e32 v68, 0
	v_mov_b32_e32 v69, 0
	v_mov_b32_e32 v86, 0
	v_mov_b32_e32 v87, 0
	v_mov_b32_e32 v88, 0
	v_mov_b32_e32 v89, 0
	s_waitcnt lgkmcnt(4)
	global_store_dwordx4 v[132:133], v[78:81], off
	v_lshl_add_u64 v[132:133], v[132:133], 0, s[100:101]
	v_cvt_pk_bf16_f32 v62, v62, v63
	v_cvt_pk_bf16_f32 v63, v64, v65
	v_cvt_pk_bf16_f32 v64, v58, v59
	v_cvt_pk_bf16_f32 v65, v60, v61
	ds_bpermute_b32 v62, v130, v62
	ds_bpermute_b32 v63, v130, v63
	ds_bpermute_b32 v64, v130, v64
	ds_bpermute_b32 v65, v130, v65
	v_mov_b32_e32 v58, 0
	v_mov_b32_e32 v59, 0
	v_mov_b32_e32 v60, 0
	v_mov_b32_e32 v61, 0
	v_mov_b32_e32 v78, 0
	v_mov_b32_e32 v79, 0
	v_mov_b32_e32 v80, 0
	v_mov_b32_e32 v81, 0
	s_waitcnt lgkmcnt(4)
	global_store_dwordx4 v[134:135], v[70:73], off
	v_lshl_add_u64 v[134:135], v[134:135], 0, s[100:101]
	v_cvt_pk_bf16_f32 v54, v54, v55
	v_cvt_pk_bf16_f32 v55, v56, v57
	v_cvt_pk_bf16_f32 v56, v50, v51
	v_cvt_pk_bf16_f32 v57, v52, v53
	ds_bpermute_b32 v54, v130, v54
	ds_bpermute_b32 v55, v130, v55
	ds_bpermute_b32 v56, v130, v56
	ds_bpermute_b32 v57, v130, v57
	v_mov_b32_e32 v50, 0
	v_mov_b32_e32 v51, 0
	v_mov_b32_e32 v52, 0
	v_mov_b32_e32 v53, 0
	v_mov_b32_e32 v70, 0
	v_mov_b32_e32 v71, 0
	v_mov_b32_e32 v72, 0
	v_mov_b32_e32 v73, 0
	s_waitcnt lgkmcnt(4)
	global_store_dwordx4 v[132:133], v[62:65], off
	v_lshl_add_u64 v[132:133], v[132:133], 0, s[98:99]
	v_cvt_pk_bf16_f32 v46, v46, v47
	v_cvt_pk_bf16_f32 v47, v48, v49
	v_cvt_pk_bf16_f32 v48, v42, v43
	v_cvt_pk_bf16_f32 v49, v44, v45
	ds_bpermute_b32 v46, v130, v46
	ds_bpermute_b32 v47, v130, v47
	ds_bpermute_b32 v48, v130, v48
	ds_bpermute_b32 v49, v130, v49
	v_mov_b32_e32 v42, 0
	v_mov_b32_e32 v43, 0
	v_mov_b32_e32 v44, 0
	v_mov_b32_e32 v45, 0
	v_mov_b32_e32 v62, 0
	v_mov_b32_e32 v63, 0
	v_mov_b32_e32 v64, 0
	v_mov_b32_e32 v65, 0
	s_waitcnt lgkmcnt(4)
	global_store_dwordx4 v[134:135], v[54:57], off
	v_lshl_add_u64 v[134:135], v[134:135], 0, s[98:99]
	v_cvt_pk_bf16_f32 v38, v38, v39
	v_cvt_pk_bf16_f32 v39, v40, v41
	v_cvt_pk_bf16_f32 v40, v34, v35
	v_cvt_pk_bf16_f32 v41, v36, v37
	ds_bpermute_b32 v38, v130, v38
	ds_bpermute_b32 v39, v130, v39
	ds_bpermute_b32 v40, v130, v40
	ds_bpermute_b32 v41, v130, v41
	v_mov_b32_e32 v34, 0
	v_mov_b32_e32 v35, 0
	v_mov_b32_e32 v36, 0
	v_mov_b32_e32 v37, 0
	v_mov_b32_e32 v54, 0
	v_mov_b32_e32 v55, 0
	v_mov_b32_e32 v56, 0
	v_mov_b32_e32 v57, 0
	s_waitcnt lgkmcnt(4)
	global_store_dwordx4 v[132:133], v[46:49], off
	v_lshl_add_u64 v[132:133], v[132:133], 0, s[98:99]
	v_cvt_pk_bf16_f32 v30, v30, v31
	v_cvt_pk_bf16_f32 v31, v32, v33
	v_cvt_pk_bf16_f32 v32, v26, v27
	v_cvt_pk_bf16_f32 v33, v28, v29
	ds_bpermute_b32 v30, v130, v30
	ds_bpermute_b32 v31, v130, v31
	ds_bpermute_b32 v32, v130, v32
	ds_bpermute_b32 v33, v130, v33
	v_mov_b32_e32 v26, 0
	v_mov_b32_e32 v27, 0
	v_mov_b32_e32 v28, 0
	v_mov_b32_e32 v29, 0
	v_mov_b32_e32 v46, 0
	v_mov_b32_e32 v47, 0
	v_mov_b32_e32 v48, 0
	v_mov_b32_e32 v49, 0
	s_waitcnt lgkmcnt(4)
	global_store_dwordx4 v[134:135], v[38:41], off
	v_lshl_add_u64 v[134:135], v[134:135], 0, s[98:99]
	v_cvt_pk_bf16_f32 v22, v22, v23
	v_cvt_pk_bf16_f32 v23, v24, v25
	v_cvt_pk_bf16_f32 v24, v18, v19
	v_cvt_pk_bf16_f32 v25, v20, v21
	ds_bpermute_b32 v22, v130, v22
	ds_bpermute_b32 v23, v130, v23
	ds_bpermute_b32 v24, v130, v24
	ds_bpermute_b32 v25, v130, v25
	v_mov_b32_e32 v18, 0
	v_mov_b32_e32 v19, 0
	v_mov_b32_e32 v20, 0
	v_mov_b32_e32 v21, 0
	v_mov_b32_e32 v38, 0
	v_mov_b32_e32 v39, 0
	v_mov_b32_e32 v40, 0
	v_mov_b32_e32 v41, 0
	s_waitcnt lgkmcnt(4)
	global_store_dwordx4 v[132:133], v[30:33], off
	v_lshl_add_u64 v[132:133], v[132:133], 0, s[98:99]
	v_cvt_pk_bf16_f32 v14, v14, v15
	v_cvt_pk_bf16_f32 v15, v16, v17
	v_cvt_pk_bf16_f32 v16, v10, v11
	v_cvt_pk_bf16_f32 v17, v12, v13
	ds_bpermute_b32 v14, v130, v14
	ds_bpermute_b32 v15, v130, v15
	ds_bpermute_b32 v16, v130, v16
	ds_bpermute_b32 v17, v130, v17
	v_mov_b32_e32 v10, 0
	v_mov_b32_e32 v11, 0
	v_mov_b32_e32 v12, 0
	v_mov_b32_e32 v13, 0
	v_mov_b32_e32 v30, 0
	v_mov_b32_e32 v31, 0
	v_mov_b32_e32 v32, 0
	v_mov_b32_e32 v33, 0
	s_waitcnt lgkmcnt(4)
	global_store_dwordx4 v[134:135], v[22:25], off
	v_lshl_add_u64 v[134:135], v[134:135], 0, s[98:99]
	v_cvt_pk_bf16_f32 v6, v6, v7
	v_cvt_pk_bf16_f32 v7, v8, v9
	v_cvt_pk_bf16_f32 v8, v2, v3
	v_cvt_pk_bf16_f32 v9, v4, v5
	ds_bpermute_b32 v6, v130, v6
	ds_bpermute_b32 v7, v130, v7
	ds_bpermute_b32 v8, v130, v8
	ds_bpermute_b32 v9, v130, v9
	v_mov_b32_e32 v2, 0
	v_mov_b32_e32 v3, 0
	v_mov_b32_e32 v4, 0
	v_mov_b32_e32 v5, 0
	v_mov_b32_e32 v22, 0
	v_mov_b32_e32 v23, 0
	v_mov_b32_e32 v24, 0
	v_mov_b32_e32 v25, 0
	s_waitcnt lgkmcnt(4)
	global_store_dwordx4 v[132:133], v[14:17], off
	v_lshl_add_u64 v[132:133], v[132:133], 0, s[98:99]
	s_waitcnt lgkmcnt(0)
	global_store_dwordx4 v[134:135], v[6:9], off
	v_mov_b32_e32 v14, 0
	v_mov_b32_e32 v15, 0
	v_mov_b32_e32 v16, 0
	v_mov_b32_e32 v17, 0
	s_nop 1
	v_mov_b32_e32 v6, 0
	v_mov_b32_e32 v7, 0
	v_mov_b32_e32 v8, 0
	v_mov_b32_e32 v9, 0
	s_mov_b32 s101, 1
	s_branch .LBB0_536
	s_cmp_lt_i32 s8, 6
	s_cselect_b64 s[36:37], -1, 0
	s_cmp_gt_i32 s8, 5
	s_cselect_b64 s[34:35], -1, 0
	s_mov_b64 s[38:39], -1
	s_and_b64 vcc, exec, s[34:35]
	v_lshlrev_b32_e32 v130, 1, v148
	s_cbranch_vccz .LBB0_540
	s_lshl_b64 s[38:39], s[30:31], 1
	s_add_u32 s38, s66, s38
	v_ashrrev_i32_e32 v159, 31, v158
	s_addc_u32 s39, s67, s39
	v_lshlrev_b64 v[132:133], 8, v[158:159]
	v_lshl_add_u64 v[132:133], s[38:39], 0, v[132:133]
	s_lshl_b32 s14, s54, 1
	v_lshl_add_u64 v[132:133], v[132:133], 0, s[14:15]
	v_mov_b32_e32 v131, v147
	v_lshl_add_u64 v[134:135], v[132:133], 0, v[130:131]
	s_mov_b64 s[38:39], 0
